# out-proj epilogue: non-temporal hint on the read-once residual (xin) loads
# speedup vs baseline: 1.0073x; 1.0054x over previous
.LBB0_728:
	s_add_i32 s13, s12, 0xffff8000
	s_and_b32 s13, s13, 0x8000
	s_add_i32 s23, s13, 0
	s_setprio 1
	s_and_b32 s13, s12, 0x8000
	s_add_i32 s13, s13, 0
	s_add_i32 s24, s13, s17
	v_lshl_add_u64 v[90:91], v[68:69], 0, s[10:11]
	s_mov_b32 m0, s24
	s_add_i32 s25, s13, s20
	global_load_lds_dwordx4 v[90:91], off
	v_lshl_add_u64 v[90:91], v[70:71], 0, s[10:11]
	s_mov_b32 m0, s25
	s_add_i32 s26, s13, s21
	global_load_lds_dwordx4 v[90:91], off
	v_lshl_add_u64 v[90:91], v[72:73], 0, s[10:11]
	s_mov_b32 m0, s26
	s_add_i32 s27, s13, s22
	global_load_lds_dwordx4 v[90:91], off
	v_lshl_add_u64 v[90:91], v[74:75], 0, s[10:11]
	s_mov_b32 m0, s27
	s_nop 0
	global_load_lds_dwordx4 v[90:91], off
	v_lshl_add_u64 v[90:91], v[76:77], 0, s[10:11]
	s_add_i32 m0, s24, 0x4000
	s_nop 0
	global_load_lds_dwordx4 v[90:91], off
	v_lshl_add_u64 v[90:91], v[78:79], 0, s[10:11]
	s_add_i32 m0, s25, 0x4000
	s_nop 0
	global_load_lds_dwordx4 v[90:91], off
	v_lshl_add_u64 v[90:91], v[80:81], 0, s[10:11]
	s_add_i32 m0, s26, 0x4000
	s_nop 0
	global_load_lds_dwordx4 v[90:91], off
	v_lshl_add_u64 v[90:91], v[82:83], 0, s[10:11]
	s_add_i32 m0, s27, 0x4000
	s_nop 0
	global_load_lds_dwordx4 v[90:91], off
	s_setprio 0
	v_add_u32_e32 v89, s23, v84
	v_add_u32_e32 v102, v89, v88
	ds_read_b128 v[90:93], v102
	v_add_u32_e32 v103, s23, v85
	v_add_u32_e32 v98, v103, v88
	ds_read_b128 v[94:97], v98 offset:16384
	ds_read_b128 v[98:101], v98 offset:20480
	s_add_u32 s10, s10, 0x80
	s_addc_u32 s11, s11, 0
	s_add_i32 s12, s12, 0x8000
	s_cmpk_lg_i32 s10, 0x780
	s_waitcnt lgkmcnt(0)
	v_mfma_f32_32x32x16_bf16 v[52:67], v[90:93], v[94:97], v[52:67]
	v_mfma_f32_32x32x16_bf16 v[20:35], v[90:93], v[98:101], v[20:35]
	ds_read_b128 v[90:93], v102 offset:4096
	v_add_u32_e32 v102, v89, v87
	s_waitcnt lgkmcnt(0)
	v_mfma_f32_32x32x16_bf16 v[36:51], v[90:93], v[94:97], v[36:51]
	v_mfma_f32_32x32x16_bf16 v[4:19], v[90:93], v[98:101], v[4:19]
	ds_read_b128 v[90:93], v102
	v_add_u32_e32 v98, v103, v87
	ds_read_b128 v[94:97], v98 offset:16384
	ds_read_b128 v[98:101], v98 offset:20480
	s_waitcnt lgkmcnt(0)
	v_mfma_f32_32x32x16_bf16 v[52:67], v[90:93], v[94:97], v[52:67]
	v_mfma_f32_32x32x16_bf16 v[20:35], v[90:93], v[98:101], v[20:35]
	ds_read_b128 v[90:93], v102 offset:4096
	v_add_u32_e32 v102, v89, v86
	v_add_u32_e32 v89, v89, v2
	s_waitcnt lgkmcnt(0)
	v_mfma_f32_32x32x16_bf16 v[36:51], v[90:93], v[94:97], v[36:51]
	v_mfma_f32_32x32x16_bf16 v[4:19], v[90:93], v[98:101], v[4:19]
	ds_read_b128 v[90:93], v102
	v_add_u32_e32 v98, v103, v86
	ds_read_b128 v[94:97], v98 offset:16384
	ds_read_b128 v[98:101], v98 offset:20480
	s_waitcnt lgkmcnt(0)
	v_mfma_f32_32x32x16_bf16 v[52:67], v[90:93], v[94:97], v[52:67]
	v_mfma_f32_32x32x16_bf16 v[20:35], v[90:93], v[98:101], v[20:35]
	ds_read_b128 v[90:93], v102 offset:4096
	s_waitcnt lgkmcnt(0)
	v_mfma_f32_32x32x16_bf16 v[36:51], v[90:93], v[94:97], v[36:51]
	v_mfma_f32_32x32x16_bf16 v[4:19], v[90:93], v[98:101], v[4:19]
	ds_read_b128 v[90:93], v89
	v_add_u32_e32 v98, v103, v2
	ds_read_b128 v[94:97], v98 offset:16384
	ds_read_b128 v[98:101], v98 offset:20480
	s_waitcnt lgkmcnt(0)
	v_mfma_f32_32x32x16_bf16 v[52:67], v[90:93], v[94:97], v[52:67]
	v_mfma_f32_32x32x16_bf16 v[20:35], v[90:93], v[98:101], v[20:35]
	ds_read_b128 v[90:93], v89 offset:4096
	s_waitcnt vmcnt(0) lgkmcnt(0)
	s_barrier
	v_mfma_f32_32x32x16_bf16 v[36:51], v[90:93], v[94:97], v[36:51]
	v_mfma_f32_32x32x16_bf16 v[4:19], v[90:93], v[98:101], v[4:19]
	s_cbranch_scc1 .LBB0_728
	s_setprio 1
	s_setprio 0
	s_add_i32 s10, s8, s35
	s_ashr_i32 s11, s10, 31
	s_lshr_b32 s11, s11, 19
	v_add_u32_e32 v84, s13, v84
	s_add_i32 s10, s10, s11
	v_add_u32_e32 v68, v84, v88
	s_ashr_i32 s10, s10, 13
	ds_read_b128 v[72:75], v68
	s_ashr_i32 s11, s10, 31
	s_add_u32 s10, s4, s10
	v_add_u32_e32 v108, s13, v85
	s_addc_u32 s11, s5, s11
	v_add_u32_e32 v69, v108, v88
	s_mulk_i32 s11, 0x6000
	s_mul_hi_u32 s12, s10, 0x6000
	ds_read_b128 v[88:91], v69 offset:16384
	ds_read_b128 v[114:117], v68 offset:4096
	ds_read_b128 v[118:121], v69 offset:20480
	s_add_i32 s12, s12, s11
	s_mulk_i32 s10, 0x6000
	s_add_u32 s10, s70, s10
	s_addc_u32 s11, s71, s12
	s_add_u32 s10, s10, 0x2000
	v_add_u32_e32 v68, v84, v87
	v_add_u32_e32 v76, v108, v87
	s_addc_u32 s11, s11, 0
	v_or_b32_e32 v142, s15, v112
	s_add_i32 s9, s9, s8
	v_lshrrev_b32_e32 v1, 3, v1
	s_waitcnt lgkmcnt(2)
	v_mfma_f32_32x32x16_bf16 v[52:67], v[72:75], v[88:91], v[52:67]
	ds_read_b128 v[122:125], v68
	ds_read_b128 v[68:71], v68 offset:4096
	v_add_u32_e32 v80, v108, v86
	v_and_or_b32 v136, v1, 4, s9
	v_lshlrev_b32_e32 v1, 2, v142
	v_ashrrev_i32_e32 v137, 31, v136
	v_lshlrev_b64 v[130:131], 12, v[136:137]
	v_or_b32_e32 v130, v130, v1
	s_waitcnt lgkmcnt(2)
	v_mfma_f32_32x32x16_bf16 v[20:35], v[72:75], v[118:121], v[20:35]
	ds_read_b128 v[100:103], v76 offset:16384
	ds_read_b128 v[72:75], v76 offset:20480
	v_add_u32_e32 v76, v84, v86
	v_add_u32_e32 v84, v84, v2
	v_add_u32_e32 v2, v108, v2
	ds_read_b128 v[92:95], v76
	ds_read_b128 v[76:79], v76 offset:4096
	ds_read_b128 v[104:107], v80 offset:16384
	ds_read_b128 v[80:83], v80 offset:20480
	ds_read_b128 v[96:99], v84
	ds_read_b128 v[84:87], v84 offset:4096
	v_mfma_f32_32x32x16_bf16 v[36:51], v[114:117], v[88:91], v[36:51]
	ds_read_b128 v[108:111], v2 offset:16384
	ds_read_b128 v[88:91], v2 offset:20480
	s_waitcnt lgkmcnt(0)
	s_barrier
	global_load_dword v126, v1, s[10:11]
	v_or_b32_e32 v2, s96, v142
	v_lshl_add_u64 v[112:113], v[2:3], 2, s[68:69]
	global_load_dword v2, v[112:113], off nt
	v_lshl_add_u64 v[112:113], s[0:1], 0, v[130:131]
	s_movk_i32 s8, 0x2000
	v_mfma_f32_32x32x16_bf16 v[4:19], v[114:117], v[118:121], v[4:19]
	v_add_co_u32_e32 v114, vcc, s8, v112
	s_mov_b32 s9, 0x9000
	s_nop 0
	v_addc_co_u32_e32 v115, vcc, 0, v113, vcc
	global_load_dword v132, v[112:113], off nt
	global_load_dword v133, v[114:115], off offset:-4096 nt
	v_add_co_u32_e32 v120, vcc, s91, v112
	s_mov_b32 s12, 0xb000
	s_nop 0
	v_addc_co_u32_e32 v121, vcc, 0, v113, vcc
	v_add_co_u32_e32 v118, vcc, s9, v112
	s_mov_b32 s13, 0x11000
	s_nop 0
	v_addc_co_u32_e32 v119, vcc, 0, v113, vcc
	v_add_co_u32_e32 v116, vcc, s12, v112
	v_mfma_f32_32x32x16_bf16 v[52:67], v[122:125], v[100:103], v[52:67]
	s_nop 0
	v_addc_co_u32_e32 v117, vcc, 0, v113, vcc
	global_load_dword v134, v[114:115], off nt
	global_load_dword v135, v[118:119], off offset:-4096 nt
	global_load_dword v137, v[118:119], off nt
	global_load_dword v138, v[116:117], off offset:-4096 nt
	global_load_dword v139, v[116:117], off nt
	global_load_dword v140, v[120:121], off nt
	s_mov_b32 s15, 0x13000
	s_mov_b32 s33, 0x1b000
	v_readlane_b32 s16, v253, 60
	v_readlane_b32 s18, v253, 62
	v_mfma_f32_32x32x16_bf16 v[20:35], v[122:125], v[72:75], v[20:35]
	v_add_co_u32_e32 v122, vcc, s13, v112
	v_readlane_b32 s19, v253, 63
	s_nop 0
	v_addc_co_u32_e32 v123, vcc, 0, v113, vcc
	global_load_dword v141, v[122:123], off offset:-4096 nt
	global_load_dword v143, v[122:123], off nt
	v_add_co_u32_e32 v124, vcc, s15, v112
	v_mfma_f32_32x32x16_bf16 v[52:67], v[92:95], v[104:107], v[52:67]
	s_nop 0
	v_addc_co_u32_e32 v125, vcc, 0, v113, vcc
	global_load_dword v144, v[124:125], off offset:-4096 nt
	global_load_dword v145, v[124:125], off nt
	v_lshl_add_u64 v[130:131], s[18:19], 0, v[130:131]
	s_mov_b32 s92, 0x18000
	v_readlane_b32 s17, v253, 61
	v_mfma_f32_32x32x16_bf16 v[52:67], v[96:99], v[108:111], v[52:67]
	v_readlane_b32 s20, v254, 0
	v_readlane_b32 s21, v254, 1
	v_readlane_b32 s22, v254, 2
	v_readlane_b32 s23, v254, 3
	v_readlane_b32 s24, v254, 4
	v_readlane_b32 s25, v254, 5
	v_readlane_b32 s26, v254, 6
	v_mfma_f32_32x32x16_bf16 v[36:51], v[68:71], v[100:103], v[36:51]
	v_readlane_b32 s27, v254, 7
	v_readlane_b32 s28, v254, 8
	v_readlane_b32 s29, v254, 9
	v_readlane_b32 s30, v254, 10
	v_readlane_b32 s31, v254, 11
	s_waitcnt vmcnt(13)
	v_add_f32_e32 v146, 1.0, v126
	v_add_co_u32_e32 v126, vcc, s86, v112
	s_waitcnt vmcnt(12)
	v_add_f32_e32 v52, v52, v2
	v_addc_co_u32_e32 v127, vcc, 0, v113, vcc
	global_load_dword v147, v[126:127], off offset:-4096 nt
	v_add_co_u32_e32 v128, vcc, s33, v112
	v_mul_f32_e32 v52, v146, v52
	s_nop 0
	v_addc_co_u32_e32 v129, vcc, 0, v113, vcc
	global_load_dword v148, v[126:127], off nt
	global_load_dword v149, v[128:129], off offset:-4096 nt
	global_load_dword v150, v[128:129], off nt
	s_waitcnt vmcnt(15)
	v_fmac_f32_e32 v52, 0x3fb504f3, v132
	global_store_dword v[130:131], v52, off
	s_waitcnt vmcnt(15)
	v_mul_f32_e32 v132, 0x3fb504f3, v133
	v_add_f32_e32 v52, v53, v2
	v_fmac_f32_e32 v132, v146, v52
	v_add_co_u32_e32 v52, vcc, s8, v130
	v_add_f32_e32 v54, v54, v2
	s_nop 0
	v_addc_co_u32_e32 v53, vcc, 0, v131, vcc
	global_store_dword v[52:53], v132, off offset:-4096
	s_waitcnt vmcnt(15)
	v_mul_f32_e32 v132, 0x3fb504f3, v134
	v_fmac_f32_e32 v132, v146, v54
	global_store_dword v[52:53], v132, off
	v_add_f32_e32 v54, v55, v2
	s_waitcnt vmcnt(11)
	v_mul_f32_e32 v132, 0x3fb504f3, v140
	v_fmac_f32_e32 v132, v146, v54
	v_add_co_u32_e32 v54, vcc, s91, v130
	v_mul_f32_e32 v134, 0x3fb504f3, v135
	s_nop 0
	v_addc_co_u32_e32 v55, vcc, 0, v131, vcc
	v_add_f32_e32 v56, v56, v2
	global_store_dword v[54:55], v132, off
	v_fmac_f32_e32 v134, v146, v56
	v_add_co_u32_e32 v132, vcc, s9, v130
	v_mul_f32_e32 v56, 0x3fb504f3, v137
	v_add_f32_e32 v57, v57, v2
	v_addc_co_u32_e32 v133, vcc, 0, v131, vcc
	v_fmac_f32_e32 v56, v146, v57
	global_store_dword v[132:133], v134, off offset:-4096
	global_store_dword v[132:133], v56, off
	v_mul_f32_e32 v134, 0x3fb504f3, v138
	v_add_f32_e32 v56, v58, v2
	v_fmac_f32_e32 v134, v146, v56
	v_add_co_u32_e32 v56, vcc, s12, v130
	v_mul_f32_e32 v58, 0x3fb504f3, v139
	v_add_f32_e32 v59, v59, v2
	v_addc_co_u32_e32 v57, vcc, 0, v131, vcc
	v_fmac_f32_e32 v58, v146, v59
	global_store_dword v[56:57], v134, off offset:-4096
	global_store_dword v[56:57], v58, off
	s_waitcnt vmcnt(15)
	v_mul_f32_e32 v134, 0x3fb504f3, v141
	v_add_f32_e32 v58, v60, v2
	v_fmac_f32_e32 v134, v146, v58
	v_add_co_u32_e32 v58, vcc, s13, v130
	s_waitcnt vmcnt(14)
	v_mul_f32_e32 v60, 0x3fb504f3, v143
	v_add_f32_e32 v61, v61, v2
	v_addc_co_u32_e32 v59, vcc, 0, v131, vcc
	v_fmac_f32_e32 v60, v146, v61
	global_store_dword v[58:59], v134, off offset:-4096
	global_store_dword v[58:59], v60, off
	s_waitcnt vmcnt(15)
	v_mul_f32_e32 v134, 0x3fb504f3, v144
	v_add_f32_e32 v60, v62, v2
	v_fmac_f32_e32 v134, v146, v60
	v_add_co_u32_e32 v60, vcc, s15, v130
	s_waitcnt vmcnt(14)
	v_mul_f32_e32 v62, 0x3fb504f3, v145
	v_add_f32_e32 v63, v63, v2
	v_addc_co_u32_e32 v61, vcc, 0, v131, vcc
	v_fmac_f32_e32 v62, v146, v63
	global_store_dword v[60:61], v134, off offset:-4096
	global_store_dword v[60:61], v62, off
	v_add_f32_e32 v63, v64, v2
	v_add_co_u32_e32 v134, vcc, s86, v130
	s_waitcnt vmcnt(15)
	v_mul_f32_e32 v62, 0x3fb504f3, v147
	v_fmac_f32_e32 v62, v146, v63
	v_addc_co_u32_e32 v135, vcc, 0, v131, vcc
	global_store_dword v[134:135], v62, off offset:-4096
	s_waitcnt vmcnt(15)
	v_mul_f32_e32 v62, 0x3fb504f3, v148
	v_add_f32_e32 v63, v65, v2
	v_fmac_f32_e32 v62, v146, v63
	global_store_dword v[134:135], v62, off
	s_waitcnt vmcnt(15)
	v_mul_f32_e32 v62, 0x3fb504f3, v149
	v_add_f32_e32 v63, v66, v2
	v_add_co_u32_e32 v64, vcc, s33, v130
	v_fmac_f32_e32 v62, v146, v63
	s_nop 0
	v_addc_co_u32_e32 v65, vcc, 0, v131, vcc
	global_store_dword v[64:65], v62, off offset:-4096
	s_waitcnt vmcnt(15)
	v_mul_f32_e32 v62, 0x3fb504f3, v150
	v_add_f32_e32 v63, v67, v2
	v_fmac_f32_e32 v62, v146, v63
	global_store_dword v[64:65], v62, off
	v_or_b32_e32 v62, 32, v136
	v_ashrrev_i32_e32 v63, 31, v62
	v_lshlrev_b64 v[144:145], 12, v[62:63]
	v_or_b32_e32 v144, v144, v1
	v_lshl_add_u64 v[62:63], s[0:1], 0, v[144:145]
	v_add_co_u32_e32 v66, vcc, s8, v62
	v_mfma_f32_32x32x16_bf16 v[36:51], v[76:79], v[104:107], v[36:51]
	s_nop 0
	v_addc_co_u32_e32 v67, vcc, 0, v63, vcc
	global_load_dword v143, v[62:63], off nt
	global_load_dword v147, v[66:67], off offset:-4096 nt
	v_add_co_u32_e32 v140, vcc, s91, v62
	v_lshl_add_u64 v[102:103], s[18:19], 0, v[144:145]
	s_nop 0
	v_addc_co_u32_e32 v141, vcc, 0, v63, vcc
	v_add_co_u32_e32 v138, vcc, s9, v62
	v_mfma_f32_32x32x16_bf16 v[36:51], v[84:87], v[108:111], v[36:51]
	s_nop 0
	v_addc_co_u32_e32 v139, vcc, 0, v63, vcc
	v_add_co_u32_e32 v136, vcc, s12, v62
	v_or_b32_e32 v1, 0x80, v1
	s_nop 0
	v_addc_co_u32_e32 v137, vcc, 0, v63, vcc
	global_load_dword v148, v[66:67], off nt
	global_load_dword v149, v[138:139], off offset:-4096 nt
	global_load_dword v150, v[138:139], off nt
	global_load_dword v151, v[136:137], off offset:-4096 nt
	global_load_dword v152, v[136:137], off nt
	global_load_dword v153, v[140:141], off nt
	v_add_co_u32_e32 v100, vcc, s13, v62
	v_add_f32_e32 v36, v36, v2
	s_nop 0
	v_addc_co_u32_e32 v101, vcc, 0, v63, vcc
	global_load_dword v154, v[100:101], off offset:-4096 nt
	global_load_dword v155, v[100:101], off nt
	v_add_co_u32_e32 v104, vcc, s15, v62
	v_add_f32_e32 v38, v38, v2
	s_nop 0
	v_addc_co_u32_e32 v105, vcc, 0, v63, vcc
	global_load_dword v156, v[104:105], off offset:-4096 nt
	global_load_dword v157, v[104:105], off nt
	v_add_co_u32_e32 v106, vcc, s86, v62
	v_add_f32_e32 v40, v40, v2
	s_nop 0
	v_addc_co_u32_e32 v107, vcc, 0, v63, vcc
	global_load_dword v158, v[106:107], off offset:-4096 nt
	v_add_co_u32_e32 v108, vcc, s33, v62
	v_add_f32_e32 v41, v41, v2
	s_nop 0
	v_addc_co_u32_e32 v109, vcc, 0, v63, vcc
	global_load_dword v159, v[106:107], off nt
	global_load_dword v160, v[108:109], off offset:-4096 nt
	global_load_dword v161, v[108:109], off nt
	v_add_f32_e32 v43, v43, v2
	v_add_f32_e32 v45, v45, v2
	v_add_f32_e32 v47, v47, v2
	v_add_f32_e32 v49, v49, v2
	v_mfma_f32_32x32x16_bf16 v[20:35], v[92:95], v[80:83], v[20:35]
	s_waitcnt vmcnt(15)
	v_mul_f32_e32 v110, 0x3fb504f3, v143
	v_fmac_f32_e32 v110, v146, v36
	global_store_dword v[102:103], v110, off
	s_waitcnt vmcnt(15)
	v_mul_f32_e32 v110, 0x3fb504f3, v147
	v_add_f32_e32 v36, v37, v2
	v_fmac_f32_e32 v110, v146, v36
	v_add_co_u32_e32 v36, vcc, s8, v102
	s_movk_i32 s8, 0x1000
	s_nop 0
	v_addc_co_u32_e32 v37, vcc, 0, v103, vcc
	global_store_dword v[36:37], v110, off offset:-4096
	s_waitcnt vmcnt(15)
	v_mul_f32_e32 v110, 0x3fb504f3, v148
	v_fmac_f32_e32 v110, v146, v38
	global_store_dword v[36:37], v110, off
	v_add_f32_e32 v38, v39, v2
	s_waitcnt vmcnt(15)
	v_mul_f32_e32 v143, 0x3fb504f3, v149
	s_waitcnt vmcnt(11)
	v_mul_f32_e32 v110, 0x3fb504f3, v153
	v_fmac_f32_e32 v110, v146, v38
	v_add_co_u32_e32 v38, vcc, s91, v102
	v_fmac_f32_e32 v143, v146, v40
	s_nop 0
	v_addc_co_u32_e32 v39, vcc, 0, v103, vcc
	global_store_dword v[38:39], v110, off
	v_add_co_u32_e32 v110, vcc, s9, v102
	v_mul_f32_e32 v40, 0x3fb504f3, v150
	s_nop 0
	v_addc_co_u32_e32 v111, vcc, 0, v103, vcc
	v_fmac_f32_e32 v40, v146, v41
	global_store_dword v[110:111], v143, off offset:-4096
	global_store_dword v[110:111], v40, off
	v_mul_f32_e32 v143, 0x3fb504f3, v151
	v_add_f32_e32 v40, v42, v2
	v_fmac_f32_e32 v143, v146, v40
	v_add_co_u32_e32 v40, vcc, s12, v102
	v_mul_f32_e32 v42, 0x3fb504f3, v152
	s_nop 0
	v_addc_co_u32_e32 v41, vcc, 0, v103, vcc
	v_fmac_f32_e32 v42, v146, v43
	global_store_dword v[40:41], v143, off offset:-4096
	global_store_dword v[40:41], v42, off
	s_waitcnt vmcnt(15)
	v_mul_f32_e32 v143, 0x3fb504f3, v154
	v_add_f32_e32 v42, v44, v2
	v_fmac_f32_e32 v143, v146, v42
	v_add_co_u32_e32 v42, vcc, s13, v102
	s_waitcnt vmcnt(14)
	v_mul_f32_e32 v44, 0x3fb504f3, v155
	v_addc_co_u32_e32 v43, vcc, 0, v103, vcc
	v_fmac_f32_e32 v44, v146, v45
	global_store_dword v[42:43], v143, off offset:-4096
	global_store_dword v[42:43], v44, off
	s_waitcnt vmcnt(15)
	v_mul_f32_e32 v143, 0x3fb504f3, v156
	v_add_f32_e32 v44, v46, v2
	v_fmac_f32_e32 v143, v146, v44
	v_add_co_u32_e32 v44, vcc, s15, v102
	s_waitcnt vmcnt(14)
	v_mul_f32_e32 v46, 0x3fb504f3, v157
	v_addc_co_u32_e32 v45, vcc, 0, v103, vcc
	v_fmac_f32_e32 v46, v146, v47
	global_store_dword v[44:45], v143, off offset:-4096
	global_store_dword v[44:45], v46, off
	s_waitcnt vmcnt(15)
	v_mul_f32_e32 v143, 0x3fb504f3, v158
	v_add_f32_e32 v46, v48, v2
	v_fmac_f32_e32 v143, v146, v46
	v_add_co_u32_e32 v46, vcc, s86, v102
	s_waitcnt vmcnt(14)
	v_mul_f32_e32 v48, 0x3fb504f3, v159
	v_addc_co_u32_e32 v47, vcc, 0, v103, vcc
	v_fmac_f32_e32 v48, v146, v49
	global_store_dword v[46:47], v143, off offset:-4096
	global_store_dword v[46:47], v48, off
	s_waitcnt vmcnt(15)
	v_mul_f32_e32 v143, 0x3fb504f3, v160
	v_add_f32_e32 v48, v50, v2
	v_fmac_f32_e32 v143, v146, v48
	v_add_co_u32_e32 v48, vcc, s33, v102
	s_waitcnt vmcnt(14)
	v_mul_f32_e32 v50, 0x3fb504f3, v161
	v_add_f32_e32 v2, v51, v2
	v_addc_co_u32_e32 v49, vcc, 0, v103, vcc
	v_fmac_f32_e32 v50, v146, v2
	global_store_dword v[48:49], v143, off offset:-4096
	global_store_dword v[48:49], v50, off
	v_add_u32_e32 v2, s96, v142
	global_load_dword v1, v1, s[10:11]
	v_lshl_add_u64 v[50:51], v[2:3], 2, s[68:69]
	global_load_dword v2, v[50:51], off offset:128 nt
	global_load_dword v142, v[112:113], off offset:128 nt
	v_add_co_u32_e32 v50, vcc, s8, v112
	s_mov_b32 s9, 0x8000
	s_nop 0
	v_addc_co_u32_e32 v51, vcc, 0, v113, vcc
	global_load_dword v143, v[50:51], off offset:128 nt
	global_load_dword v144, v[114:115], off offset:128 nt
	v_add_co_u32_e32 v50, vcc, s9, v112
	global_load_dword v120, v[120:121], off offset:128 nt
	s_nop 0
	v_addc_co_u32_e32 v51, vcc, 0, v113, vcc
	global_load_dword v121, v[50:51], off offset:128 nt
	s_nop 0
	global_load_dword v118, v[118:119], off offset:128 nt
	s_mov_b32 s12, 0xa000
	v_add_co_u32_e32 v50, vcc, s12, v112
	s_mov_b32 s10, 0x10000
	s_nop 0
	v_addc_co_u32_e32 v51, vcc, 0, v113, vcc
	global_load_dword v119, v[50:51], off offset:128 nt
	s_mov_b32 s11, 0x12000
	global_load_dword v116, v[116:117], off offset:128 nt
	v_add_co_u32_e32 v50, vcc, s10, v112
	s_mov_b32 s13, 0x18000
	s_nop 0
	v_addc_co_u32_e32 v51, vcc, 0, v113, vcc
	global_load_dword v117, v[50:51], off offset:128 nt
	v_add_co_u32_e32 v50, vcc, s11, v112
	v_mfma_f32_32x32x16_bf16 v[20:35], v[96:99], v[88:91], v[20:35]
	s_nop 0
	v_addc_co_u32_e32 v51, vcc, 0, v113, vcc
	global_load_dword v122, v[122:123], off offset:128 nt
	s_nop 0
	global_load_dword v123, v[50:51], off offset:128 nt
	v_add_co_u32_e32 v50, vcc, s13, v112
	global_load_dword v124, v[124:125], off offset:128 nt
	s_nop 0
	v_addc_co_u32_e32 v51, vcc, 0, v113, vcc
	global_load_dword v125, v[50:51], off offset:128 nt
	v_add_co_u32_e32 v92, vcc, s93, v112
	v_mfma_f32_32x32x16_bf16 v[4:19], v[68:71], v[72:75], v[4:19]
	s_nop 0
	v_addc_co_u32_e32 v93, vcc, 0, v113, vcc
	global_load_dword v126, v[126:127], off offset:128 nt
	s_nop 0
	global_load_dword v127, v[92:93], off offset:128 nt
	v_add_co_u32_e32 v50, vcc, s8, v130
	global_load_dword v128, v[128:129], off offset:128 nt
	s_nop 0
	v_addc_co_u32_e32 v51, vcc, 0, v131, vcc
	v_add_co_u32_e32 v92, vcc, s9, v130
	v_mfma_f32_32x32x16_bf16 v[4:19], v[76:79], v[80:83], v[4:19]
	s_nop 0
	v_addc_co_u32_e32 v93, vcc, 0, v131, vcc
	v_add_co_u32_e32 v94, vcc, s12, v130
	s_waitcnt vmcnt(17)
	v_add_f32_e32 v1, 1.0, v1
	s_waitcnt vmcnt(16)
	v_add_f32_e32 v20, v20, v2
	v_mul_f32_e32 v20, v1, v20
	s_waitcnt vmcnt(15)
	v_fmac_f32_e32 v20, 0x3fb504f3, v142
	global_store_dword v[130:131], v20, off offset:128
	v_add_f32_e32 v21, v21, v2
	v_addc_co_u32_e32 v95, vcc, 0, v131, vcc
	s_waitcnt vmcnt(15)
	v_mul_f32_e32 v20, 0x3fb504f3, v143
	v_fmac_f32_e32 v20, v1, v21
	global_store_dword v[50:51], v20, off offset:128
	s_waitcnt vmcnt(15)
	v_mul_f32_e32 v20, 0x3fb504f3, v144
	v_add_f32_e32 v21, v22, v2
	v_fmac_f32_e32 v20, v1, v21
	global_store_dword v[52:53], v20, off offset:128
	s_waitcnt vmcnt(15)
	v_mul_f32_e32 v20, 0x3fb504f3, v120
	v_add_f32_e32 v21, v23, v2
	v_fmac_f32_e32 v20, v1, v21
	global_store_dword v[54:55], v20, off offset:128
	s_waitcnt vmcnt(15)
	v_mul_f32_e32 v20, 0x3fb504f3, v121
	v_add_f32_e32 v21, v24, v2
	v_fmac_f32_e32 v20, v1, v21
	global_store_dword v[92:93], v20, off offset:128
	s_waitcnt vmcnt(15)
	v_mul_f32_e32 v20, 0x3fb504f3, v118
	v_add_f32_e32 v21, v25, v2
	v_fmac_f32_e32 v20, v1, v21
	global_store_dword v[132:133], v20, off offset:128
	s_waitcnt vmcnt(15)
	v_mul_f32_e32 v20, 0x3fb504f3, v119
	v_add_f32_e32 v21, v26, v2
	v_fmac_f32_e32 v20, v1, v21
	global_store_dword v[94:95], v20, off offset:128
	s_waitcnt vmcnt(15)
	v_mul_f32_e32 v20, 0x3fb504f3, v116
	v_add_f32_e32 v21, v27, v2
	v_fmac_f32_e32 v20, v1, v21
	v_add_co_u32_e32 v96, vcc, s10, v130
	global_store_dword v[56:57], v20, off offset:128
	s_waitcnt vmcnt(15)
	v_mul_f32_e32 v20, 0x3fb504f3, v117
	v_add_f32_e32 v21, v28, v2
	v_addc_co_u32_e32 v97, vcc, 0, v131, vcc
	v_fmac_f32_e32 v20, v1, v21
	global_store_dword v[96:97], v20, off offset:128
	s_waitcnt vmcnt(15)
	v_mul_f32_e32 v20, 0x3fb504f3, v122
	v_add_f32_e32 v21, v29, v2
	v_fmac_f32_e32 v20, v1, v21
	v_add_co_u32_e32 v98, vcc, s11, v130
	global_store_dword v[58:59], v20, off offset:128
	s_waitcnt vmcnt(15)
	v_mul_f32_e32 v20, 0x3fb504f3, v123
	v_add_f32_e32 v21, v30, v2
	v_addc_co_u32_e32 v99, vcc, 0, v131, vcc
	v_fmac_f32_e32 v20, v1, v21
	global_store_dword v[98:99], v20, off offset:128
	s_waitcnt vmcnt(15)
	v_mul_f32_e32 v20, 0x3fb504f3, v124
	v_add_f32_e32 v21, v31, v2
	v_fmac_f32_e32 v20, v1, v21
	v_add_co_u32_e32 v112, vcc, s13, v130
	global_store_dword v[60:61], v20, off offset:128
	s_waitcnt vmcnt(15)
	v_mul_f32_e32 v20, 0x3fb504f3, v125
	v_add_f32_e32 v21, v32, v2
	v_addc_co_u32_e32 v113, vcc, 0, v131, vcc
	v_fmac_f32_e32 v20, v1, v21
	global_store_dword v[112:113], v20, off offset:128
	s_waitcnt vmcnt(15)
	v_mul_f32_e32 v20, 0x3fb504f3, v126
	v_add_f32_e32 v21, v33, v2
	v_fmac_f32_e32 v20, v1, v21
	v_add_co_u32_e32 v114, vcc, s93, v130
	global_store_dword v[134:135], v20, off offset:128
	s_waitcnt vmcnt(15)
	v_mul_f32_e32 v20, 0x3fb504f3, v127
	v_add_f32_e32 v21, v34, v2
	v_addc_co_u32_e32 v115, vcc, 0, v131, vcc
	v_fmac_f32_e32 v20, v1, v21
	global_store_dword v[114:115], v20, off offset:128
	s_waitcnt vmcnt(15)
	v_mul_f32_e32 v20, 0x3fb504f3, v128
	v_add_f32_e32 v21, v35, v2
	v_fmac_f32_e32 v20, v1, v21
	global_store_dword v[64:65], v20, off offset:128
	global_load_dword v34, v[62:63], off offset:128 nt
	v_add_co_u32_e32 v20, vcc, s8, v62
	v_mfma_f32_32x32x16_bf16 v[4:19], v[84:87], v[88:91], v[4:19]
	s_nop 0
	v_addc_co_u32_e32 v21, vcc, 0, v63, vcc
	global_load_dword v35, v[20:21], off offset:128 nt
	global_load_dword v50, v[66:67], off offset:128 nt
	global_load_dword v51, v[140:141], off offset:128 nt
	global_load_dword v55, v[136:137], off offset:128 nt
	v_add_co_u32_e32 v20, vcc, s9, v62
	global_load_dword v53, v[138:139], off offset:128 nt
	s_nop 0
	v_addc_co_u32_e32 v21, vcc, 0, v63, vcc
	global_load_dword v52, v[20:21], off offset:128 nt
	v_add_co_u32_e32 v20, vcc, s12, v62
	v_add_f32_e32 v4, v4, v2
	s_nop 0
	v_addc_co_u32_e32 v21, vcc, 0, v63, vcc
	global_load_dword v54, v[20:21], off offset:128 nt
	v_add_co_u32_e32 v20, vcc, s10, v62
	v_add_f32_e32 v5, v5, v2
	s_nop 0
	v_addc_co_u32_e32 v21, vcc, 0, v63, vcc
	global_load_dword v56, v[20:21], off offset:128 nt
	global_load_dword v57, v[100:101], off offset:128 nt
	v_add_co_u32_e32 v20, vcc, s11, v62
	global_load_dword v59, v[104:105], off offset:128 nt
	s_nop 0
	v_addc_co_u32_e32 v21, vcc, 0, v63, vcc
	global_load_dword v58, v[20:21], off offset:128 nt
	v_add_co_u32_e32 v20, vcc, s13, v62
	s_waitcnt vmcnt(11)
	v_mul_f32_e32 v34, 0x3fb504f3, v34
	v_addc_co_u32_e32 v21, vcc, 0, v63, vcc
	global_load_dword v60, v[20:21], off offset:128 nt
	global_load_dword v61, v[106:107], off offset:128 nt
	v_add_co_u32_e32 v22, vcc, s93, v62
	v_fmac_f32_e32 v34, v1, v4
	s_nop 0
	v_addc_co_u32_e32 v23, vcc, 0, v63, vcc
	global_load_dword v62, v[108:109], off offset:128 nt
	global_load_dword v63, v[22:23], off offset:128 nt
	v_add_co_u32_e32 v20, vcc, s8, v102
	s_waitcnt vmcnt(14)
	v_mul_f32_e32 v4, 0x3fb504f3, v35
	v_addc_co_u32_e32 v21, vcc, 0, v103, vcc
	v_fmac_f32_e32 v4, v1, v5
	global_store_dword v[20:21], v4, off offset:128
	s_waitcnt vmcnt(14)
	v_mul_f32_e32 v4, 0x3fb504f3, v50
	v_add_f32_e32 v5, v6, v2
	v_fmac_f32_e32 v4, v1, v5
	global_store_dword v[36:37], v4, off offset:128
	s_waitcnt vmcnt(14)
	v_mul_f32_e32 v4, 0x3fb504f3, v51
	v_add_f32_e32 v5, v7, v2
	v_fmac_f32_e32 v4, v1, v5
	v_add_co_u32_e32 v22, vcc, s9, v102
	global_store_dword v[38:39], v4, off offset:128
	s_waitcnt vmcnt(12)
	v_mul_f32_e32 v4, 0x3fb504f3, v52
	v_add_f32_e32 v5, v8, v2
	v_addc_co_u32_e32 v23, vcc, 0, v103, vcc
	v_fmac_f32_e32 v4, v1, v5
	global_store_dword v[22:23], v4, off offset:128
	v_mul_f32_e32 v4, 0x3fb504f3, v53
	v_add_f32_e32 v5, v9, v2
	v_fmac_f32_e32 v4, v1, v5
	v_add_co_u32_e32 v24, vcc, s12, v102
	global_store_dword v[110:111], v4, off offset:128
	s_waitcnt vmcnt(13)
	v_mul_f32_e32 v4, 0x3fb504f3, v54
	v_add_f32_e32 v5, v10, v2
	v_addc_co_u32_e32 v25, vcc, 0, v103, vcc
	v_fmac_f32_e32 v4, v1, v5
	global_store_dword v[24:25], v4, off offset:128
	v_mul_f32_e32 v4, 0x3fb504f3, v55
	v_add_f32_e32 v5, v11, v2
	v_fmac_f32_e32 v4, v1, v5
	v_add_co_u32_e32 v26, vcc, s10, v102
	global_store_dword v[40:41], v4, off offset:128
	s_waitcnt vmcnt(14)
	v_mul_f32_e32 v4, 0x3fb504f3, v56
	v_add_f32_e32 v5, v12, v2
	v_addc_co_u32_e32 v27, vcc, 0, v103, vcc
	v_fmac_f32_e32 v4, v1, v5
	global_store_dword v[26:27], v4, off offset:128
	s_waitcnt vmcnt(14)
	v_mul_f32_e32 v4, 0x3fb504f3, v57
	v_add_f32_e32 v5, v13, v2
	v_fmac_f32_e32 v4, v1, v5
	v_add_co_u32_e32 v28, vcc, s11, v102
	global_store_dword v[42:43], v4, off offset:128
	s_waitcnt vmcnt(13)
	v_mul_f32_e32 v4, 0x3fb504f3, v58
	v_add_f32_e32 v5, v14, v2
	v_addc_co_u32_e32 v29, vcc, 0, v103, vcc
	v_fmac_f32_e32 v4, v1, v5
	global_store_dword v[28:29], v4, off offset:128
	v_mul_f32_e32 v4, 0x3fb504f3, v59
	v_add_f32_e32 v5, v15, v2
	v_fmac_f32_e32 v4, v1, v5
	v_add_co_u32_e32 v30, vcc, s13, v102
	global_store_dword v[44:45], v4, off offset:128
	v_add_f32_e32 v5, v16, v2
	v_addc_co_u32_e32 v31, vcc, 0, v103, vcc
	v_add_co_u32_e32 v32, vcc, s93, v102
	global_store_dword v[102:103], v34, off offset:128
	s_nop 0
	v_addc_co_u32_e32 v33, vcc, 0, v103, vcc
	s_waitcnt vmcnt(15)
	v_mul_f32_e32 v4, 0x3fb504f3, v60
	v_fmac_f32_e32 v4, v1, v5
	global_store_dword v[30:31], v4, off offset:128
	s_waitcnt vmcnt(15)
	v_mul_f32_e32 v4, 0x3fb504f3, v61
	v_add_f32_e32 v5, v17, v2
	v_fmac_f32_e32 v4, v1, v5
	global_store_dword v[46:47], v4, off offset:128
	s_waitcnt vmcnt(14)
	v_mul_f32_e32 v4, 0x3fb504f3, v63
	v_add_f32_e32 v5, v18, v2
	v_fmac_f32_e32 v4, v1, v5
	global_store_dword v[32:33], v4, off offset:128
	v_mul_f32_e32 v4, 0x3fb504f3, v62
	v_add_f32_e32 v2, v19, v2
	v_fmac_f32_e32 v4, v1, v2
	global_store_dword v[48:49], v4, off offset:128
	v_mov_b32_e32 v1, s36
	ds_read_b32 v2, v1
	s_load_dword s8, s[94:95], 0x0
	ds_read_b32 v1, v1
	s_waitcnt lgkmcnt(0)
	v_readfirstlane_b32 s10, v2
	s_ashr_i32 s9, s8, 31
	s_lshr_b32 s9, s9, 29
	s_add_i32 s9, s8, s9
	s_ashr_i32 s9, s9, 3
	s_cmp_eq_u32 s10, 0
	s_cselect_b32 s8, s8, s9
	v_cmp_eq_u32_e32 vcc, 0, v1
	s_add_i32 s2, s8, s2
	s_nop 0
	v_cndmask_b32_e32 v1, v207, v208, vcc
	v_cmp_ge_i32_e32 vcc, s2, v1
	s_cbranch_vccz .LBB0_725
